# conversion loops: counted vmcnt waits (half-tile loads stay in flight), finer stagger (8 points in P2, 5 in P3)
# speedup vs baseline: 1.0541x; 1.0091x over previous
.LBB0_157:
	s_cmp_lt_i32 s46, 3
	s_cselect_b64 s[0:1], -1, 0
	s_and_b64 s[6:7], s[0:1], s[6:7]
	s_andn2_b64 vcc, exec, s[6:7]
	s_cbranch_vccnz .LBB0_244
	s_mov_b64 s[4:5], s[52:53]
	v_mov_b32_e32 v1, v0
	s_load_dwordx4 s[8:11], s[4:5], 0xd0
	s_and_b32 s0, s78, 7
	s_branch .LBB0_163
	s_cmp_lt_i32 s0, 1
	s_cbranch_scc1 .LBB0_163
	s_cmp_eq_u32 s0, 1
	s_cbranch_scc1 .LBB0_161
	s_cmp_eq_u32 s0, 2
	s_cselect_b32 s0, 5, 8
	s_cbranch_execz .LBB0_162
	s_branch .LBB0_163

.LBB0_200:
	s_mul_i32 s22, s97, 0x2400
	s_add_i32 s22, s22, 0
	s_add_u32 s26, s26, s30
	s_addc_u32 s27, s27, 0
	s_mov_b32 s25, 0
	s_lshl_b64 s[26:27], s[26:27], s24
	s_lshl_b32 s24, s29, 2
	s_waitcnt vmcnt(29)
	v_lshl_add_u64 v[10:11], v[132:133], 0, s[24:25]
	s_lshl_b32 s24, s29, 3
	v_lshl_add_u64 v[12:13], v[132:133], 0, s[24:25]
	s_mul_i32 s24, s29, 12
	s_waitcnt vmcnt(26)
	v_lshl_add_u64 v[18:19], v[132:133], 0, s[24:25]
	s_lshl_b32 s24, s29, 4
	v_lshl_add_u64 v[20:21], v[132:133], 0, s[24:25]
	s_mul_i32 s24, s29, 20
	s_waitcnt vmcnt(25)
	v_lshl_add_u64 v[26:27], v[132:133], 0, s[24:25]
	s_mul_i32 s24, s29, 24
	v_lshl_add_u64 v[28:29], v[132:133], 0, s[24:25]
	s_mul_i32 s24, s29, 28
	s_waitcnt vmcnt(23)
	v_lshl_add_u64 v[34:35], v[132:133], 0, s[24:25]
	s_lshl_b32 s24, s29, 5
	v_lshl_add_u64 v[36:37], v[132:133], 0, s[24:25]
	s_mul_i32 s24, s29, 36
	s_waitcnt vmcnt(21)
	v_lshl_add_u64 v[42:43], v[132:133], 0, s[24:25]
	s_mul_i32 s24, s29, 40
	v_lshl_add_u64 v[44:45], v[132:133], 0, s[24:25]
	s_mul_i32 s24, s29, 44
	s_waitcnt vmcnt(19)
	v_lshl_add_u64 v[50:51], v[132:133], 0, s[24:25]
	s_mul_i32 s24, s29, 48
	v_lshl_add_u64 v[52:53], v[132:133], 0, s[24:25]
	s_mul_i32 s24, s29, 52
	s_add_u32 s4, s10, s4
	global_load_dwordx4 v[2:5], v[10:11], off
	global_load_dwordx4 v[6:9], v[12:13], off
	s_nop 0
	global_load_dwordx4 v[10:13], v[18:19], off
	global_load_dwordx4 v[14:17], v[20:21], off
	s_nop 0
	global_load_dwordx4 v[18:21], v[26:27], off
	global_load_dwordx4 v[22:25], v[28:29], off
	s_nop 0
	global_load_dwordx4 v[26:29], v[34:35], off
	global_load_dwordx4 v[30:33], v[36:37], off
	s_nop 0
	global_load_dwordx4 v[34:37], v[42:43], off
	global_load_dwordx4 v[38:41], v[44:45], off
	s_nop 0
	global_load_dwordx4 v[42:45], v[50:51], off
	global_load_dwordx4 v[46:49], v[52:53], off
	v_lshl_add_u64 v[50:51], v[132:133], 0, s[24:25]
	s_mul_i32 s24, s29, 56
	s_addc_u32 s5, s11, s5
	v_lshl_add_u64 v[52:53], v[132:133], 0, s[24:25]
	s_mul_i32 s24, s29, 60
	s_add_u32 s4, s4, s26
	s_waitcnt vmcnt(28)
	v_lshl_add_u64 v[62:63], v[132:133], 0, s[24:25]
	s_addc_u32 s5, s5, s27
	s_lshl_b32 s24, s29, 8
	v_lshl_add_u64 v[64:65], v[132:133], 0, s[24:25]
	s_mul_i32 s24, s29, 0x104
	v_lshl_add_u64 v[74:75], v[132:133], 0, s[24:25]
	s_mul_i32 s24, s29, 0x108
	v_lshl_add_u64 v[76:77], v[132:133], 0, s[24:25]
	s_mul_i32 s24, s29, 0x10c
	v_lshl_add_u64 v[82:83], v[132:133], 0, s[24:25]
	s_mul_i32 s24, s29, 0x110
	v_lshl_add_u64 v[84:85], v[132:133], 0, s[24:25]
	s_mul_i32 s24, s29, 0x114
	v_lshl_add_u64 v[90:91], v[132:133], 0, s[24:25]
	s_mul_i32 s24, s29, 0x118
	v_lshl_add_u64 v[92:93], v[132:133], 0, s[24:25]
	s_mul_i32 s24, s29, 0x11c
	v_lshl_add_u64 v[98:99], v[132:133], 0, s[24:25]
	s_mul_i32 s24, s29, 0x120
	v_lshl_add_u64 v[100:101], v[132:133], 0, s[24:25]
	s_mul_i32 s24, s29, 0x124
	v_lshl_add_u64 v[106:107], v[132:133], 0, s[24:25]
	s_mul_i32 s24, s29, 0x128
	v_lshl_add_u64 v[108:109], v[132:133], 0, s[24:25]
	s_mul_i32 s24, s29, 0x12c
	global_load_dwordx4 v[54:57], v[50:51], off
	global_load_dwordx4 v[58:61], v[52:53], off
	global_load_dwordx4 v[70:73], v[62:63], off
	s_nop 0
	global_load_dwordx4 v[50:53], v[64:65], off
	s_nop 0
	global_load_dwordx4 v[62:65], v[74:75], off
	global_load_dwordx4 v[66:69], v[76:77], off
	s_nop 0
	global_load_dwordx4 v[74:77], v[82:83], off
	global_load_dwordx4 v[78:81], v[84:85], off
	s_nop 0
	global_load_dwordx4 v[82:85], v[90:91], off
	global_load_dwordx4 v[86:89], v[92:93], off
	s_nop 0
	global_load_dwordx4 v[90:93], v[98:99], off
	global_load_dwordx4 v[94:97], v[100:101], off
	s_nop 0
	global_load_dwordx4 v[98:101], v[106:107], off
	global_load_dwordx4 v[102:105], v[108:109], off
	v_lshl_add_u64 v[106:107], v[132:133], 0, s[24:25]
	s_mul_i32 s24, s29, 0x130
	v_lshl_add_u64 v[108:109], v[132:133], 0, s[24:25]
	s_mul_i32 s24, s29, 0x134
	global_load_dwordx4 v[110:113], v[106:107], off
	global_load_dwordx4 v[114:117], v[108:109], off
	v_lshl_add_u64 v[106:107], v[132:133], 0, s[24:25]
	s_mul_i32 s24, s29, 0x138
	v_lshl_add_u64 v[108:109], v[132:133], 0, s[24:25]
	s_mul_i32 s24, s29, 0x13c
	v_lshl_add_u64 v[126:127], v[132:133], 0, s[24:25]
	global_load_dwordx4 v[118:121], v[106:107], off
	global_load_dwordx4 v[122:125], v[108:109], off
	s_nop 0
	global_load_dwordx4 v[106:109], v[132:133], off
	s_nop 0
	global_load_dwordx4 v[126:129], v[126:127], off
	v_bfe_u32 v134, v1, 3, 3
	v_lshlrev_b32_e32 v1, 4, v1
	s_add_u32 s26, s4, s28
	v_and_b32_e32 v136, 0x70, v1
	s_movk_i32 s4, 0x90
	v_mov_b32_e32 v1, s22
	s_addc_u32 s27, s5, 0
	v_add_u32_e32 v146, s22, v135
	v_add_u32_e32 v148, s22, v136
	v_mov_b32_e32 v139, 0
	v_mul_i32_i24_e32 v147, 0x90, v138
	v_mad_i32_i24 v138, v138, s4, v1
	v_mul_u32_u24_e32 v149, 0x90, v134
	s_add_i32 s4, s96, s33
	v_mov_b32_e32 v137, v139
	v_or_b32_e32 v140, 8, v134
	v_or_b32_e32 v142, 16, v134
	v_or_b32_e32 v144, 24, v134
	v_or_b32_e32 v1, 32, v134
	v_or_b32_e32 v141, 40, v134
	v_or_b32_e32 v143, 48, v134
	v_or_b32_e32 v145, 56, v134
	s_lshl_b32 s22, s4, 6
	s_lshl_b32 s40, s96, 6
	s_lshl_b32 s41, s4, 5
	s_lshl_b32 s42, s96, 5
	s_lshl_b32 s43, s4, 3
	s_lshl_b32 s44, s96, 3
	s_mov_b32 s45, 0xc3e00000
	v_add_u32_e32 v146, v146, v147
	v_add_u32_e32 v147, v138, v135
	v_add_u32_e32 v148, v148, v149
	v_mov_b32_e32 v149, 0x43e00000
	s_mov_b32 s24, s29
	s_mov_b32 s47, s33
	s_mov_b64 s[34:35], s[26:27]
	s_mov_b32 s30, s18
	s_waitcnt vmcnt(0)
	s_branch .LBB0_202

.LBB0_209:
	s_waitcnt vmcnt(24)
	v_mul_f32_e32 v138, 0x42800000, v106
	v_mul_f32_e32 v150, 0x42800000, v2
	v_med3_f32 v138, v138, s45, v149
	v_med3_f32 v152, v150, s45, v149
	v_mov_b32_e32 v150, 0
	v_cvt_pk_fp8_f32 v150, v138, v152
	v_mul_f32_e32 v151, 0x42800000, v6
	v_mul_f32_e32 v138, 0x42800000, v10
	v_med3_f32 v151, v151, s45, v149
	v_med3_f32 v138, v138, s45, v149
	v_cvt_pk_fp8_f32 v150, v151, v138 op_sel:[0,0,1]
	v_mul_f32_e32 v138, 0x42800000, v14
	v_mul_f32_e32 v151, 0x42800000, v18
	v_med3_f32 v138, v138, s45, v149
	v_med3_f32 v153, v151, s45, v149
	v_mov_b32_e32 v151, 0
	v_cvt_pk_fp8_f32 v151, v138, v153
	v_mul_f32_e32 v152, 0x42800000, v22
	v_mul_f32_e32 v138, 0x42800000, v26
	v_med3_f32 v152, v152, s45, v149
	v_med3_f32 v138, v138, s45, v149
	v_cvt_pk_fp8_f32 v151, v152, v138 op_sel:[0,0,1]
	v_mul_f32_e32 v138, 0x42800000, v30
	v_mul_f32_e32 v152, 0x42800000, v34
	v_med3_f32 v138, v138, s45, v149
	v_med3_f32 v154, v152, s45, v149
	v_mov_b32_e32 v152, 0
	v_cvt_pk_fp8_f32 v152, v138, v154
	v_mul_f32_e32 v153, 0x42800000, v38
	v_mul_f32_e32 v138, 0x42800000, v42
	v_med3_f32 v153, v153, s45, v149
	v_med3_f32 v138, v138, s45, v149
	v_cvt_pk_fp8_f32 v152, v153, v138 op_sel:[0,0,1]
	v_mul_f32_e32 v138, 0x42800000, v46
	v_mul_f32_e32 v153, 0x42800000, v54
	v_med3_f32 v138, v138, s45, v149
	v_med3_f32 v155, v153, s45, v149
	v_mov_b32_e32 v153, 0
	v_cvt_pk_fp8_f32 v153, v138, v155
	v_mul_f32_e32 v154, 0x42800000, v58
	v_mul_f32_e32 v138, 0x42800000, v70
	v_med3_f32 v154, v154, s45, v149
	v_med3_f32 v138, v138, s45, v149
	v_cvt_pk_fp8_f32 v153, v154, v138 op_sel:[0,0,1]
	v_mul_f32_e32 v138, 0x42800000, v107
	v_mul_f32_e32 v154, 0x42800000, v3
	v_med3_f32 v138, v138, s45, v149
	v_med3_f32 v156, v154, s45, v149
	v_mov_b32_e32 v154, 0
	v_cvt_pk_fp8_f32 v154, v138, v156
	v_mul_f32_e32 v155, 0x42800000, v7
	v_mul_f32_e32 v138, 0x42800000, v11
	v_med3_f32 v155, v155, s45, v149
	v_med3_f32 v138, v138, s45, v149
	v_cvt_pk_fp8_f32 v154, v155, v138 op_sel:[0,0,1]
	v_mul_f32_e32 v138, 0x42800000, v15
	v_mul_f32_e32 v155, 0x42800000, v19
	v_med3_f32 v138, v138, s45, v149
	v_med3_f32 v157, v155, s45, v149
	v_mov_b32_e32 v155, 0
	v_cvt_pk_fp8_f32 v155, v138, v157
	v_mul_f32_e32 v156, 0x42800000, v23
	v_mul_f32_e32 v138, 0x42800000, v27
	v_med3_f32 v156, v156, s45, v149
	v_med3_f32 v138, v138, s45, v149
	v_cvt_pk_fp8_f32 v155, v156, v138 op_sel:[0,0,1]
	v_mul_f32_e32 v138, 0x42800000, v31
	v_mul_f32_e32 v156, 0x42800000, v35
	v_med3_f32 v138, v138, s45, v149
	v_med3_f32 v158, v156, s45, v149
	v_mov_b32_e32 v156, 0
	v_cvt_pk_fp8_f32 v156, v138, v158
	v_mul_f32_e32 v157, 0x42800000, v39
	v_mul_f32_e32 v138, 0x42800000, v43
	v_med3_f32 v157, v157, s45, v149
	v_med3_f32 v138, v138, s45, v149
	v_cvt_pk_fp8_f32 v156, v157, v138 op_sel:[0,0,1]
	v_mul_f32_e32 v138, 0x42800000, v47
	v_mul_f32_e32 v157, 0x42800000, v55
	v_med3_f32 v138, v138, s45, v149
	v_med3_f32 v159, v157, s45, v149
	v_mov_b32_e32 v157, 0
	v_cvt_pk_fp8_f32 v157, v138, v159
	v_mul_f32_e32 v158, 0x42800000, v59
	v_mul_f32_e32 v138, 0x42800000, v71
	v_med3_f32 v158, v158, s45, v149
	v_med3_f32 v138, v138, s45, v149
	v_cvt_pk_fp8_f32 v157, v158, v138 op_sel:[0,0,1]
	v_mul_f32_e32 v138, 0x42800000, v108
	v_mul_f32_e32 v158, 0x42800000, v4
	v_med3_f32 v138, v138, s45, v149
	v_med3_f32 v160, v158, s45, v149
	v_mov_b32_e32 v158, 0
	v_cvt_pk_fp8_f32 v158, v138, v160
	v_mul_f32_e32 v159, 0x42800000, v8
	v_mul_f32_e32 v138, 0x42800000, v12
	v_med3_f32 v159, v159, s45, v149
	v_med3_f32 v138, v138, s45, v149
	v_cvt_pk_fp8_f32 v158, v159, v138 op_sel:[0,0,1]
	v_mul_f32_e32 v138, 0x42800000, v16
	v_mul_f32_e32 v159, 0x42800000, v20
	v_med3_f32 v138, v138, s45, v149
	v_med3_f32 v161, v159, s45, v149
	v_mov_b32_e32 v159, 0
	v_cvt_pk_fp8_f32 v159, v138, v161
	v_mul_f32_e32 v160, 0x42800000, v24
	v_mul_f32_e32 v138, 0x42800000, v28
	v_med3_f32 v160, v160, s45, v149
	v_med3_f32 v138, v138, s45, v149
	v_cvt_pk_fp8_f32 v159, v160, v138 op_sel:[0,0,1]
	v_mul_f32_e32 v138, 0x42800000, v32
	v_mul_f32_e32 v160, 0x42800000, v36
	v_med3_f32 v138, v138, s45, v149
	v_med3_f32 v162, v160, s45, v149
	v_mov_b32_e32 v160, 0
	v_cvt_pk_fp8_f32 v160, v138, v162
	v_mul_f32_e32 v161, 0x42800000, v40
	v_mul_f32_e32 v138, 0x42800000, v44
	v_med3_f32 v161, v161, s45, v149
	v_med3_f32 v138, v138, s45, v149
	v_cvt_pk_fp8_f32 v160, v161, v138 op_sel:[0,0,1]
	v_mul_f32_e32 v138, 0x42800000, v48
	v_mul_f32_e32 v161, 0x42800000, v56
	v_med3_f32 v138, v138, s45, v149
	v_med3_f32 v163, v161, s45, v149
	v_mov_b32_e32 v161, 0
	v_cvt_pk_fp8_f32 v161, v138, v163
	v_mul_f32_e32 v162, 0x42800000, v60
	v_mul_f32_e32 v138, 0x42800000, v72
	v_med3_f32 v162, v162, s45, v149
	v_med3_f32 v138, v138, s45, v149
	v_cvt_pk_fp8_f32 v161, v162, v138 op_sel:[0,0,1]
	ds_write_b128 v146, v[150:153]
	ds_write_b128 v146, v[154:157] offset:144
	ds_write_b128 v146, v[158:161] offset:288
	v_mul_f32_e32 v138, 0x42800000, v109
	v_mul_f32_e32 v150, 0x42800000, v5
	v_med3_f32 v138, v138, s45, v149
	v_med3_f32 v152, v150, s45, v149
	v_mov_b32_e32 v150, 0
	v_cvt_pk_fp8_f32 v150, v138, v152
	v_mul_f32_e32 v151, 0x42800000, v9
	v_mul_f32_e32 v138, 0x42800000, v13
	v_med3_f32 v151, v151, s45, v149
	v_med3_f32 v138, v138, s45, v149
	v_cvt_pk_fp8_f32 v150, v151, v138 op_sel:[0,0,1]
	v_mul_f32_e32 v138, 0x42800000, v17
	v_mul_f32_e32 v151, 0x42800000, v21
	v_med3_f32 v138, v138, s45, v149
	v_med3_f32 v153, v151, s45, v149
	v_mov_b32_e32 v151, 0
	v_cvt_pk_fp8_f32 v151, v138, v153
	v_mul_f32_e32 v152, 0x42800000, v25
	v_mul_f32_e32 v138, 0x42800000, v29
	v_med3_f32 v152, v152, s45, v149
	v_med3_f32 v138, v138, s45, v149
	v_cvt_pk_fp8_f32 v151, v152, v138 op_sel:[0,0,1]
	v_mul_f32_e32 v138, 0x42800000, v33
	v_mul_f32_e32 v152, 0x42800000, v37
	v_med3_f32 v138, v138, s45, v149
	v_med3_f32 v154, v152, s45, v149
	v_mov_b32_e32 v152, 0
	v_cvt_pk_fp8_f32 v152, v138, v154
	v_mul_f32_e32 v153, 0x42800000, v41
	v_mul_f32_e32 v138, 0x42800000, v45
	v_med3_f32 v153, v153, s45, v149
	v_med3_f32 v138, v138, s45, v149
	v_cvt_pk_fp8_f32 v152, v153, v138 op_sel:[0,0,1]
	v_mul_f32_e32 v138, 0x42800000, v49
	v_mul_f32_e32 v153, 0x42800000, v57
	v_med3_f32 v138, v138, s45, v149
	v_med3_f32 v155, v153, s45, v149
	v_mov_b32_e32 v153, 0
	v_cvt_pk_fp8_f32 v153, v138, v155
	v_mul_f32_e32 v154, 0x42800000, v61
	v_mul_f32_e32 v138, 0x42800000, v73
	v_med3_f32 v154, v154, s45, v149
	v_med3_f32 v138, v138, s45, v149
	v_cvt_pk_fp8_f32 v153, v154, v138 op_sel:[0,0,1]
	v_cndmask_b32_e64 v138, 0, 1, s[36:37]
	v_cmp_ne_u32_e64 s[4:5], 1, v138
	s_andn2_b64 vcc, exec, s[36:37]
	ds_write_b128 v146, v[150:153] offset:432
	s_cbranch_vccnz .Lcv2_nomore
	s_lshl_b64 s[36:37], s[24:25], 2
	v_lshl_add_u64 v[2:3], v[132:133], 0, s[36:37]
	v_lshl_add_u64 v[10:11], v[2:3], 0, s[36:37]
	global_load_dwordx4 v[106:109], v[132:133], off
	s_nop 0
	global_load_dwordx4 v[2:5], v[2:3], off
	s_nop 0
	global_load_dwordx4 v[6:9], v[10:11], off
	v_lshl_add_u64 v[10:11], v[10:11], 0, s[36:37]
	v_lshl_add_u64 v[18:19], v[10:11], 0, s[36:37]
	global_load_dwordx4 v[10:13], v[10:11], off
	s_nop 0
	global_load_dwordx4 v[14:17], v[18:19], off
	v_lshl_add_u64 v[18:19], v[18:19], 0, s[36:37]
	v_lshl_add_u64 v[26:27], v[18:19], 0, s[36:37]
	global_load_dwordx4 v[18:21], v[18:19], off
	s_nop 0
	global_load_dwordx4 v[22:25], v[26:27], off
	v_lshl_add_u64 v[26:27], v[26:27], 0, s[36:37]
	v_lshl_add_u64 v[34:35], v[26:27], 0, s[36:37]
	global_load_dwordx4 v[26:29], v[26:27], off
	s_nop 0
	global_load_dwordx4 v[30:33], v[34:35], off
	v_lshl_add_u64 v[34:35], v[34:35], 0, s[36:37]
	v_lshl_add_u64 v[42:43], v[34:35], 0, s[36:37]
	v_lshl_add_u64 v[46:47], v[42:43], 0, s[36:37]
	v_lshl_add_u64 v[54:55], v[46:47], 0, s[36:37]
	v_lshl_add_u64 v[58:59], v[54:55], 0, s[36:37]
	v_lshl_add_u64 v[70:71], v[58:59], 0, s[36:37]
	global_load_dwordx4 v[34:37], v[34:35], off
	s_nop 0
	global_load_dwordx4 v[38:41], v[42:43], off
	s_nop 0
	global_load_dwordx4 v[42:45], v[46:47], off
	s_nop 0
	global_load_dwordx4 v[46:49], v[54:55], off
	s_nop 0
	global_load_dwordx4 v[54:57], v[58:59], off
	s_nop 0
	global_load_dwordx4 v[58:61], v[70:71], off
	v_lshl_add_u64 v[70:71], v[70:71], 0, s[36:37]
	global_load_dwordx4 v[70:73], v[70:71], off
	s_waitcnt vmcnt(16)
	s_branch .LBB0_211

.LBB0_211:
	v_mul_f32_e32 v138, 0x42800000, v50
	v_mul_f32_e32 v150, 0x42800000, v62
	v_med3_f32 v138, v138, s45, v149
	v_med3_f32 v152, v150, s45, v149
	v_mov_b32_e32 v150, 0
	v_cvt_pk_fp8_f32 v150, v138, v152
	v_mul_f32_e32 v151, 0x42800000, v66
	v_mul_f32_e32 v138, 0x42800000, v74
	v_med3_f32 v151, v151, s45, v149
	v_med3_f32 v138, v138, s45, v149
	v_cvt_pk_fp8_f32 v150, v151, v138 op_sel:[0,0,1]
	v_mul_f32_e32 v138, 0x42800000, v78
	v_mul_f32_e32 v151, 0x42800000, v82
	v_med3_f32 v138, v138, s45, v149
	v_med3_f32 v153, v151, s45, v149
	v_mov_b32_e32 v151, 0
	v_cvt_pk_fp8_f32 v151, v138, v153
	v_mul_f32_e32 v152, 0x42800000, v86
	v_mul_f32_e32 v138, 0x42800000, v90
	v_med3_f32 v152, v152, s45, v149
	v_med3_f32 v138, v138, s45, v149
	v_cvt_pk_fp8_f32 v151, v152, v138 op_sel:[0,0,1]
	v_mul_f32_e32 v138, 0x42800000, v94
	v_mul_f32_e32 v152, 0x42800000, v98
	v_med3_f32 v138, v138, s45, v149
	v_med3_f32 v154, v152, s45, v149
	v_mov_b32_e32 v152, 0
	v_cvt_pk_fp8_f32 v152, v138, v154
	v_mul_f32_e32 v153, 0x42800000, v102
	v_mul_f32_e32 v138, 0x42800000, v110
	v_med3_f32 v153, v153, s45, v149
	v_med3_f32 v138, v138, s45, v149
	v_cvt_pk_fp8_f32 v152, v153, v138 op_sel:[0,0,1]
	v_mul_f32_e32 v138, 0x42800000, v114
	v_mul_f32_e32 v153, 0x42800000, v118
	v_med3_f32 v138, v138, s45, v149
	v_med3_f32 v155, v153, s45, v149
	v_mov_b32_e32 v153, 0
	v_cvt_pk_fp8_f32 v153, v138, v155
	v_mul_f32_e32 v154, 0x42800000, v122
	s_nop 0
	v_mul_f32_e32 v138, 0x42800000, v126
	v_med3_f32 v154, v154, s45, v149
	v_med3_f32 v138, v138, s45, v149
	v_cvt_pk_fp8_f32 v153, v154, v138 op_sel:[0,0,1]
	v_mul_f32_e32 v138, 0x42800000, v51
	v_med3_f32 v138, v138, s45, v149
	s_and_b64 vcc, exec, s[4:5]
	ds_write_b128 v147, v[150:153] offset:64
	v_mul_f32_e32 v150, 0x42800000, v63
	v_med3_f32 v152, v150, s45, v149
	v_mov_b32_e32 v150, 0
	v_cvt_pk_fp8_f32 v150, v138, v152
	v_mul_f32_e32 v151, 0x42800000, v67
	v_mul_f32_e32 v138, 0x42800000, v75
	v_med3_f32 v151, v151, s45, v149
	v_med3_f32 v138, v138, s45, v149
	v_cvt_pk_fp8_f32 v150, v151, v138 op_sel:[0,0,1]
	v_mul_f32_e32 v138, 0x42800000, v79
	v_mul_f32_e32 v151, 0x42800000, v83
	v_med3_f32 v138, v138, s45, v149
	v_med3_f32 v153, v151, s45, v149
	v_mov_b32_e32 v151, 0
	v_cvt_pk_fp8_f32 v151, v138, v153
	v_mul_f32_e32 v152, 0x42800000, v87
	v_mul_f32_e32 v138, 0x42800000, v91
	v_med3_f32 v152, v152, s45, v149
	v_med3_f32 v138, v138, s45, v149
	v_cvt_pk_fp8_f32 v151, v152, v138 op_sel:[0,0,1]
	v_mul_f32_e32 v138, 0x42800000, v95
	v_mul_f32_e32 v152, 0x42800000, v99
	v_med3_f32 v138, v138, s45, v149
	v_med3_f32 v154, v152, s45, v149
	v_mov_b32_e32 v152, 0
	v_cvt_pk_fp8_f32 v152, v138, v154
	v_mul_f32_e32 v153, 0x42800000, v103
	v_mul_f32_e32 v138, 0x42800000, v111
	v_med3_f32 v153, v153, s45, v149
	v_med3_f32 v138, v138, s45, v149
	v_cvt_pk_fp8_f32 v152, v153, v138 op_sel:[0,0,1]
	v_mul_f32_e32 v138, 0x42800000, v115
	v_mul_f32_e32 v153, 0x42800000, v119
	v_med3_f32 v138, v138, s45, v149
	v_med3_f32 v155, v153, s45, v149
	v_mov_b32_e32 v153, 0
	v_cvt_pk_fp8_f32 v153, v138, v155
	v_mul_f32_e32 v154, 0x42800000, v123
	v_mul_f32_e32 v138, 0x42800000, v127
	v_med3_f32 v154, v154, s45, v149
	v_med3_f32 v138, v138, s45, v149
	v_cvt_pk_fp8_f32 v153, v154, v138 op_sel:[0,0,1]
	v_mul_f32_e32 v138, 0x42800000, v52
	v_mul_f32_e32 v154, 0x42800000, v64
	v_med3_f32 v138, v138, s45, v149
	v_med3_f32 v156, v154, s45, v149
	v_mov_b32_e32 v154, 0
	v_cvt_pk_fp8_f32 v154, v138, v156
	v_mul_f32_e32 v155, 0x42800000, v68
	v_mul_f32_e32 v138, 0x42800000, v76
	v_med3_f32 v155, v155, s45, v149
	v_med3_f32 v138, v138, s45, v149
	v_cvt_pk_fp8_f32 v154, v155, v138 op_sel:[0,0,1]
	v_mul_f32_e32 v138, 0x42800000, v80
	v_mul_f32_e32 v155, 0x42800000, v84
	v_med3_f32 v138, v138, s45, v149
	v_med3_f32 v157, v155, s45, v149
	v_mov_b32_e32 v155, 0
	v_cvt_pk_fp8_f32 v155, v138, v157
	v_mul_f32_e32 v156, 0x42800000, v88
	v_mul_f32_e32 v138, 0x42800000, v92
	v_med3_f32 v156, v156, s45, v149
	v_med3_f32 v138, v138, s45, v149
	v_cvt_pk_fp8_f32 v155, v156, v138 op_sel:[0,0,1]
	v_mul_f32_e32 v138, 0x42800000, v96
	v_mul_f32_e32 v156, 0x42800000, v100
	v_med3_f32 v138, v138, s45, v149
	v_med3_f32 v158, v156, s45, v149
	v_mov_b32_e32 v156, 0
	v_cvt_pk_fp8_f32 v156, v138, v158
	v_mul_f32_e32 v157, 0x42800000, v104
	v_mul_f32_e32 v138, 0x42800000, v112
	v_med3_f32 v157, v157, s45, v149
	v_med3_f32 v138, v138, s45, v149
	v_cvt_pk_fp8_f32 v156, v157, v138 op_sel:[0,0,1]
	v_mul_f32_e32 v138, 0x42800000, v116
	v_mul_f32_e32 v157, 0x42800000, v120
	v_med3_f32 v138, v138, s45, v149
	v_med3_f32 v159, v157, s45, v149
	v_mov_b32_e32 v157, 0
	v_cvt_pk_fp8_f32 v157, v138, v159
	v_mul_f32_e32 v158, 0x42800000, v124
	v_mul_f32_e32 v138, 0x42800000, v128
	v_med3_f32 v158, v158, s45, v149
	v_med3_f32 v138, v138, s45, v149
	v_cvt_pk_fp8_f32 v157, v158, v138 op_sel:[0,0,1]
	v_mul_f32_e32 v138, 0x42800000, v53
	v_mul_f32_e32 v158, 0x42800000, v65
	v_med3_f32 v138, v138, s45, v149
	v_med3_f32 v160, v158, s45, v149
	v_mov_b32_e32 v158, 0
	v_cvt_pk_fp8_f32 v158, v138, v160
	v_mul_f32_e32 v159, 0x42800000, v69
	v_mul_f32_e32 v138, 0x42800000, v77
	v_med3_f32 v159, v159, s45, v149
	v_med3_f32 v138, v138, s45, v149
	v_cvt_pk_fp8_f32 v158, v159, v138 op_sel:[0,0,1]
	v_mul_f32_e32 v138, 0x42800000, v81
	v_mul_f32_e32 v159, 0x42800000, v85
	v_med3_f32 v138, v138, s45, v149
	v_med3_f32 v161, v159, s45, v149
	v_mov_b32_e32 v159, 0
	v_cvt_pk_fp8_f32 v159, v138, v161
	v_mul_f32_e32 v160, 0x42800000, v89
	v_mul_f32_e32 v138, 0x42800000, v93
	v_med3_f32 v160, v160, s45, v149
	v_med3_f32 v138, v138, s45, v149
	v_cvt_pk_fp8_f32 v159, v160, v138 op_sel:[0,0,1]
	v_mul_f32_e32 v138, 0x42800000, v97
	v_mul_f32_e32 v160, 0x42800000, v101
	v_med3_f32 v138, v138, s45, v149
	v_med3_f32 v162, v160, s45, v149
	v_mov_b32_e32 v160, 0
	v_cvt_pk_fp8_f32 v160, v138, v162
	v_mul_f32_e32 v161, 0x42800000, v105
	v_mul_f32_e32 v138, 0x42800000, v113
	v_med3_f32 v161, v161, s45, v149
	v_med3_f32 v138, v138, s45, v149
	v_cvt_pk_fp8_f32 v160, v161, v138 op_sel:[0,0,1]
	v_mul_f32_e32 v138, 0x42800000, v117
	v_mul_f32_e32 v161, 0x42800000, v121
	v_med3_f32 v138, v138, s45, v149
	v_med3_f32 v163, v161, s45, v149
	v_mov_b32_e32 v161, 0
	v_cvt_pk_fp8_f32 v161, v138, v163
	v_mul_f32_e32 v162, 0x42800000, v125
	v_mul_f32_e32 v138, 0x42800000, v129
	v_med3_f32 v162, v162, s45, v149
	v_med3_f32 v138, v138, s45, v149
	v_cvt_pk_fp8_f32 v161, v162, v138 op_sel:[0,0,1]
	ds_write_b128 v147, v[150:153] offset:208
	ds_write_b128 v147, v[154:157] offset:352
	ds_write_b128 v147, v[158:161] offset:496
	s_cbranch_vccnz .LBB0_201
	s_lshl_b64 s[4:5], s[24:25], 8
	v_lshl_add_u64 v[50:51], v[132:133], 0, s[4:5]
	s_lshl_b64 s[4:5], s[24:25], 2
	v_lshl_add_u64 v[66:67], v[50:51], 0, s[4:5]
	global_load_dwordx4 v[50:53], v[50:51], off
	s_nop 0
	global_load_dwordx4 v[62:65], v[66:67], off
	v_lshl_add_u64 v[66:67], v[66:67], 0, s[4:5]
	v_lshl_add_u64 v[78:79], v[66:67], 0, s[4:5]
	global_load_dwordx4 v[66:69], v[66:67], off
	s_nop 0
	global_load_dwordx4 v[74:77], v[78:79], off
	v_lshl_add_u64 v[78:79], v[78:79], 0, s[4:5]
	v_lshl_add_u64 v[86:87], v[78:79], 0, s[4:5]
	global_load_dwordx4 v[78:81], v[78:79], off
	s_nop 0
	global_load_dwordx4 v[82:85], v[86:87], off
	v_lshl_add_u64 v[86:87], v[86:87], 0, s[4:5]
	v_lshl_add_u64 v[94:95], v[86:87], 0, s[4:5]
	global_load_dwordx4 v[86:89], v[86:87], off
	s_nop 0
	global_load_dwordx4 v[90:93], v[94:95], off
	v_lshl_add_u64 v[94:95], v[94:95], 0, s[4:5]
	v_lshl_add_u64 v[102:103], v[94:95], 0, s[4:5]
	v_lshl_add_u64 v[110:111], v[102:103], 0, s[4:5]
	v_lshl_add_u64 v[114:115], v[110:111], 0, s[4:5]
	v_lshl_add_u64 v[118:119], v[114:115], 0, s[4:5]
	v_lshl_add_u64 v[122:123], v[118:119], 0, s[4:5]
	v_lshl_add_u64 v[126:127], v[122:123], 0, s[4:5]
	global_load_dwordx4 v[94:97], v[94:95], off
	s_nop 0
	global_load_dwordx4 v[98:101], v[102:103], off
	s_nop 0
	global_load_dwordx4 v[102:105], v[110:111], off
	s_nop 0
	global_load_dwordx4 v[110:113], v[114:115], off
	s_nop 0
	global_load_dwordx4 v[114:117], v[118:119], off
	s_nop 0
	global_load_dwordx4 v[118:121], v[122:123], off
	s_nop 0
	global_load_dwordx4 v[122:125], v[126:127], off
	v_lshl_add_u64 v[126:127], v[126:127], 0, s[4:5]
	global_load_dwordx4 v[126:129], v[126:127], off
	s_branch .LBB0_201

.LBB0_321:
	s_cmp_lt_i32 s73, 0
	s_mov_b32 s45, 0
	s_cbranch_scc1 .LBB0_463
	s_and_b32 s0, s78, 3
	s_mul_i32 s0, s73, s0
	s_mul_hi_u32 s0, s0, 0xaaaaaaab
	s_lshr_b32 s75, s0, 1
	s_cmp_lg_u32 s73, 4
	s_cbranch_scc1 .Lstag3_done
	s_mul_i32 s0, s78, 0xcccd
	s_lshr_b32 s0, s0, 18
	s_mul_i32 s0, s0, 5
	s_sub_i32 s75, s78, s0
.Lstag3_done:
	s_mul_i32 s0, s97, 0x2400
	s_add_i32 s79, s0, 0
	s_add_i32 s46, s33, 0x2000
	s_cmpk_lt_i32 s33, 0x4000
	s_mul_hi_i32 s4, s46, 0x2aaaaaab
	s_cselect_b64 s[0:1], -1, 0
	s_lshr_b32 s5, s4, 31
	s_ashr_i32 s4, s4, 4
	s_add_i32 s4, s4, s5
	s_mul_i32 s5, s4, 0x60
	s_sub_i32 s8, s46, s5
	s_cmp_lt_i32 s8, 64
	v_writelane_b32 v255, s38, 11
	s_cselect_b64 s[6:7], -1, 0
	s_lshl_b32 s10, s8, 6
	v_writelane_b32 v255, s39, 12
	s_and_b32 s5, s10, 0x3c0
	v_writelane_b32 v255, s5, 13
	s_lshl_b32 s5, s8, 3
	s_and_b32 s5, s5, 0x7fffff80
	s_addk_i32 s5, 0xfe00
	v_writelane_b32 v255, s5, 14
	s_ashr_i32 s5, s4, 31
	s_lshl_b64 s[12:13], s[4:5], 20
	v_writelane_b32 v255, s12, 15
	s_and_b32 s9, s10, 0x300
	v_cndmask_b32_e64 v2, 0, 1, s[0:1]
	v_writelane_b32 v255, s13, 16
	s_lshl_b64 s[12:13], s[4:5], 10
	s_or_b32 s12, s12, s9
	v_writelane_b32 v255, s12, 17
	s_lshl_b32 s9, s8, 5
	s_and_b32 s11, s9, 0x60
	v_writelane_b32 v255, s13, 18
	v_writelane_b32 v255, s11, 19
	s_and_b32 s11, s10, 0xc0
	s_and_b32 s9, s9, 0x380
	s_cmp_lt_i32 s8, 32
	s_cselect_b64 s[12:13], -1, 0
	s_lshl_b32 s8, s8, 7
	v_writelane_b32 v255, s11, 20
	s_lshl_b64 s[4:5], s[4:5], 9
	s_and_b32 s8, s8, 0x100
	v_writelane_b32 v255, s9, 21
	s_or_b32 s4, s4, s8
	v_writelane_b32 v255, s12, 22
	s_and_b64 s[8:9], s[12:13], exec
	s_cselect_b32 s44, 0, 0x80
	v_writelane_b32 v255, s13, 23
	s_or_b64 s[4:5], s[4:5], s[44:45]
	v_writelane_b32 v255, s4, 24
	s_mov_b32 s8, s97
	v_mov_b32_e32 v3, 0
	v_writelane_b32 v255, s5, 25
	s_and_b32 s4, s10, 64
	v_writelane_b32 v255, s4, 26
	s_ashr_i32 s4, s78, 1
	v_writelane_b32 v255, s4, 27
	s_mov_b32 s4, s78
	v_writelane_b32 v255, s4, 28
	s_bitcmp1_b32 s78, 0
	s_mov_b32 s48, 0xc3e00000
	v_writelane_b32 v255, s5, 29
	s_cselect_b64 s[4:5], -1, 0
	v_writelane_b32 v255, s4, 30
	s_lshl_b32 s97, s97, 5
	s_lshl_b32 s89, s8, 3
	v_writelane_b32 v255, s5, 31
	s_lshl_b32 s4, s8, 13
	s_add_i32 s61, s4, 0
	s_lshl_b32 s4, s8, 1
	s_or_b32 s4, s4, 1
	s_lshl_b32 s5, s8, 4
	s_and_b32 s92, s5, 0x3fffffe0
	s_lshl_b32 s5, s4, 4
	s_and_b32 s91, s5, 48
	s_lshl_b32 s52, s8, 11
	s_add_i32 s5, 0, 0x8000
	s_lshl_b32 s94, s4, 10
	s_lshr_b32 s60, s3, 7
	s_add_i32 s61, s61, 0x10000
	s_and_b32 s90, s97, 32
	s_addk_i32 s92, 0x600
	s_or_b32 s93, s89, 4
	s_add_i32 s53, s52, s5
	s_add_i32 s76, s94, s5
	s_cmpk_gt_u32 s3, 0xff
	s_cselect_b64 s[56:57], -1, 0
	s_add_i32 s77, s52, 0
	s_cmpk_gt_u32 s3, 0x17f
	s_cselect_b64 s[58:59], -1, 0
	s_cmpk_lt_u32 s3, 0x2c0
	s_cselect_b64 s[4:5], -1, 0
	v_writelane_b32 v255, s4, 32
	s_lshl_b32 s3, s8, 7
	s_sub_i32 s3, 0, s3
	v_writelane_b32 v255, s5, 33
	v_writelane_b32 v255, s8, 34
	s_not_b32 s4, s97
	v_writelane_b32 v255, s4, 35
	v_cmp_ne_u32_e64 s[4:5], 1, v2
	v_cndmask_b32_e64 v2, 0, 1, s[6:7]
	v_cmp_ne_u32_e64 s[0:1], 1, v2
	s_movk_i32 s51, 0xf0
	s_add_i32 s49, 0, 0x203f0
	v_writelane_b32 v255, s0, 36
	s_mov_b32 s54, 0x3f4ccccd
	v_mov_b32_e32 v202, 0x43e00000
	v_writelane_b32 v255, s1, 37
	s_movk_i32 s1, 0xf000
	s_mov_b32 s0, 0x41000000
	s_mov_b32 s55, 0
	s_branch .LBB0_326

.LBB0_332:
	v_and_b32_e32 v136, -16, v134
	v_readlane_b32 s18, v255, 15
	v_add_u32_e32 v4, s6, v136
	v_readlane_b32 s19, v255, 16
	s_add_u32 s16, s16, s18
	v_ashrrev_i32_e32 v5, 31, v4
	s_addc_u32 s17, s17, s19
	v_lshlrev_b64 v[4:5], s12, v[4:5]
	v_lshlrev_b32_e32 v2, 2, v134
	v_lshl_add_u64 v[4:5], s[16:17], 0, v[4:5]
	s_lshl_b32 s44, s13, 2
	v_and_b32_e32 v146, 60, v2
	v_lshl_add_u64 v[4:5], v[4:5], 0, s[44:45]
	v_lshlrev_b32_e32 v2, 2, v146
	s_add_u32 s12, s14, s7
	v_lshl_add_u64 v[132:133], v[4:5], 0, v[2:3]
	s_addc_u32 s13, s15, 0
	s_lshl_b32 s44, s24, 2
	v_lshl_add_u64 v[4:5], v[132:133], 0, s[44:45]
	s_lshl_b32 s44, s24, 3
	v_lshl_add_u64 v[8:9], v[132:133], 0, s[44:45]
	s_mul_i32 s44, s24, 12
	v_lshl_add_u64 v[12:13], v[132:133], 0, s[44:45]
	s_lshl_b32 s44, s24, 4
	v_lshl_add_u64 v[16:17], v[132:133], 0, s[44:45]
	s_mul_i32 s44, s24, 20
	v_lshl_add_u64 v[20:21], v[132:133], 0, s[44:45]
	s_mul_i32 s44, s24, 24
	v_lshl_add_u64 v[24:25], v[132:133], 0, s[44:45]
	s_mul_i32 s44, s24, 28
	v_lshl_add_u64 v[28:29], v[132:133], 0, s[44:45]
	s_lshl_b32 s44, s24, 5
	v_lshl_add_u64 v[32:33], v[132:133], 0, s[44:45]
	s_mul_i32 s44, s24, 36
	v_lshl_add_u64 v[36:37], v[132:133], 0, s[44:45]
	s_mul_i32 s44, s24, 40
	v_lshl_add_u64 v[40:41], v[132:133], 0, s[44:45]
	s_mul_i32 s44, s24, 44
	s_lshl_b64 s[10:11], s[12:13], s10
	v_lshl_add_u64 v[44:45], v[132:133], 0, s[44:45]
	s_mul_i32 s44, s24, 48
	v_lshl_add_u64 v[48:49], v[132:133], 0, s[44:45]
	s_mul_i32 s44, s24, 52
	s_add_u32 s7, s30, s8
	s_waitcnt vmcnt(23)
	v_lshl_add_u64 v[52:53], v[132:133], 0, s[44:45]
	s_mul_i32 s44, s24, 56
	s_addc_u32 s8, s31, s9
	v_lshl_add_u64 v[54:55], v[132:133], 0, s[44:45]
	s_mul_i32 s44, s24, 60
	s_add_u32 s7, s7, s10
	global_load_dwordx4 v[4:7], v[4:5], off
	s_nop 0
	global_load_dwordx4 v[8:11], v[8:9], off
	s_nop 0
	global_load_dwordx4 v[12:15], v[12:13], off
	s_nop 0
	global_load_dwordx4 v[16:19], v[16:17], off
	s_nop 0
	global_load_dwordx4 v[20:23], v[20:21], off
	s_nop 0
	global_load_dwordx4 v[24:27], v[24:25], off
	s_nop 0
	global_load_dwordx4 v[28:31], v[28:29], off
	s_nop 0
	global_load_dwordx4 v[32:35], v[32:33], off
	s_nop 0
	global_load_dwordx4 v[36:39], v[36:37], off
	s_nop 0
	global_load_dwordx4 v[40:43], v[40:41], off
	s_nop 0
	global_load_dwordx4 v[44:47], v[44:45], off
	s_nop 0
	global_load_dwordx4 v[48:51], v[48:49], off
	s_nop 0
	global_load_dwordx4 v[56:59], v[52:53], off
	global_load_dwordx4 v[64:67], v[54:55], off
	v_lshl_add_u64 v[52:53], v[132:133], 0, s[44:45]
	s_addc_u32 s8, s8, s11
	s_lshl_b32 s44, s24, 8
	v_lshl_add_u64 v[54:55], v[132:133], 0, s[44:45]
	s_mul_i32 s44, s24, 0x104
	s_waitcnt vmcnt(36)
	v_lshl_add_u64 v[60:61], v[132:133], 0, s[44:45]
	s_mul_i32 s44, s24, 0x108
	s_waitcnt vmcnt(35)
	v_lshl_add_u64 v[68:69], v[132:133], 0, s[44:45]
	s_mul_i32 s44, s24, 0x10c
	s_waitcnt vmcnt(34)
	v_lshl_add_u64 v[72:73], v[132:133], 0, s[44:45]
	s_mul_i32 s44, s24, 0x110
	s_waitcnt vmcnt(33)
	v_lshl_add_u64 v[80:81], v[132:133], 0, s[44:45]
	s_mul_i32 s44, s24, 0x114
	s_waitcnt vmcnt(32)
	v_lshl_add_u64 v[84:85], v[132:133], 0, s[44:45]
	s_mul_i32 s44, s24, 0x118
	s_waitcnt vmcnt(31)
	v_lshl_add_u64 v[88:89], v[132:133], 0, s[44:45]
	s_mul_i32 s44, s24, 0x11c
	s_waitcnt vmcnt(30)
	v_lshl_add_u64 v[92:93], v[132:133], 0, s[44:45]
	s_mul_i32 s44, s24, 0x120
	s_waitcnt vmcnt(29)
	v_lshl_add_u64 v[96:97], v[132:133], 0, s[44:45]
	s_mul_i32 s44, s24, 0x124
	s_waitcnt vmcnt(28)
	v_lshl_add_u64 v[100:101], v[132:133], 0, s[44:45]
	s_mul_i32 s44, s24, 0x128
	v_lshl_add_u64 v[104:105], v[132:133], 0, s[44:45]
	s_mul_i32 s44, s24, 0x12c
	global_load_dwordx4 v[76:79], v[52:53], off
	s_nop 0
	global_load_dwordx4 v[52:55], v[54:55], off
	s_nop 0
	global_load_dwordx4 v[60:63], v[60:61], off
	s_nop 0
	global_load_dwordx4 v[68:71], v[68:69], off
	s_nop 0
	global_load_dwordx4 v[72:75], v[72:73], off
	s_nop 0
	global_load_dwordx4 v[80:83], v[80:81], off
	s_nop 0
	global_load_dwordx4 v[84:87], v[84:85], off
	s_nop 0
	global_load_dwordx4 v[88:91], v[88:89], off
	s_nop 0
	global_load_dwordx4 v[92:95], v[92:93], off
	s_nop 0
	global_load_dwordx4 v[96:99], v[96:97], off
	s_nop 0
	global_load_dwordx4 v[100:103], v[100:101], off
	s_nop 0
	global_load_dwordx4 v[108:111], v[104:105], off
	v_lshl_add_u64 v[104:105], v[132:133], 0, s[44:45]
	s_mul_i32 s44, s24, 0x130
	v_lshl_add_u64 v[106:107], v[132:133], 0, s[44:45]
	s_mul_i32 s44, s24, 0x134
	global_load_dwordx4 v[112:115], v[104:105], off
	global_load_dwordx4 v[116:119], v[106:107], off
	v_lshl_add_u64 v[104:105], v[132:133], 0, s[44:45]
	s_mul_i32 s44, s24, 0x138
	v_lshl_add_u64 v[106:107], v[132:133], 0, s[44:45]
	s_mul_i32 s44, s24, 0x13c
	s_waitcnt vmcnt(36)
	v_lshl_add_u64 v[128:129], v[132:133], 0, s[44:45]
	global_load_dwordx4 v[120:123], v[104:105], off
	global_load_dwordx4 v[124:127], v[106:107], off
	s_nop 0
	global_load_dwordx4 v[104:107], v[132:133], off
	s_nop 0
	global_load_dwordx4 v[128:131], v[128:129], off
	v_lshlrev_b32_e32 v2, 4, v134
	s_add_u32 s64, s7, s6
	v_ashrrev_i32_e32 v137, 3, v134
	v_and_b32_e32 v134, 0x70, v2
	v_mov_b32_e32 v2, s79
	s_movk_i32 s6, 0x90
	v_mad_u32_u24 v149, v146, s6, v2
	v_mul_lo_u32 v150, v137, s6
	s_movk_i32 s6, 0xffef
	s_addc_u32 s65, s8, 0
	v_add_u32_e32 v145, s79, v136
	v_add_u32_e32 v147, s79, v134
	v_mul_u32_u24_e32 v148, 0x90, v146
	v_cmp_lt_i32_e64 s[20:21], s6, v137
	s_movk_i32 s6, 0xffe7
	s_add_i32 s25, s96, s46
	v_mov_b32_e32 v135, v3
	v_cmp_lt_i32_e64 s[8:9], 31, v137
	v_add_u32_e32 v138, 8, v137
	v_cmp_lt_i32_e64 s[10:11], 23, v137
	v_add_u32_e32 v139, 16, v137
	v_cmp_lt_i32_e64 s[12:13], 15, v137
	v_add_u32_e32 v140, 24, v137
	v_cmp_lt_i32_e64 s[14:15], 7, v137
	v_add_u32_e32 v141, 32, v137
	v_cmp_gt_i32_e64 s[16:17], 0, v137
	v_add_u32_e32 v142, 40, v137
	v_cmp_lt_i32_e64 s[18:19], -9, v137
	v_add_u32_e32 v143, 48, v137
	v_add_u32_e32 v144, 56, v137
	v_cmp_lt_i32_e64 s[22:23], s6, v137
	s_lshl_b32 s50, s25, 6
	s_lshl_b32 s6, s96, 6
	s_lshl_b32 s7, s25, 5
	s_lshl_b32 s95, s96, 5
	s_lshl_b32 s26, s25, 3
	s_lshl_b32 s27, s96, 3
	v_lshlrev_b32_e32 v2, 2, v146
	v_add_u32_e32 v145, v145, v148
	v_add_u32_e32 v146, v149, v136
	v_add_u32_e32 v147, v147, v150
	s_mov_b32 s44, s24
	s_mov_b32 s88, s46
	s_mov_b64 s[82:83], s[64:65]
	s_mov_b32 s47, s74
	s_waitcnt vmcnt(0)
	s_branch .LBB0_334

.LBB0_341:
	s_waitcnt vmcnt(24)
	v_mul_f32_e32 v148, 0x42800000, v104
	v_mul_f32_e32 v149, 0x42800000, v4
	v_med3_f32 v151, v148, s48, v202
	v_med3_f32 v149, v149, s48, v202
	v_mov_b32_e32 v148, v3
	v_cvt_pk_fp8_f32 v148, v151, v149
	v_mul_f32_e32 v150, 0x42800000, v8
	v_mul_f32_e32 v149, 0x42800000, v12
	v_med3_f32 v150, v150, s48, v202
	v_med3_f32 v149, v149, s48, v202
	v_cvt_pk_fp8_f32 v148, v150, v149 op_sel:[0,0,1]
	v_mul_f32_e32 v149, 0x42800000, v16
	v_mul_f32_e32 v150, 0x42800000, v20
	v_med3_f32 v152, v149, s48, v202
	v_med3_f32 v150, v150, s48, v202
	v_mov_b32_e32 v149, v3
	v_cvt_pk_fp8_f32 v149, v152, v150
	v_mul_f32_e32 v151, 0x42800000, v24
	v_mul_f32_e32 v150, 0x42800000, v28
	v_med3_f32 v151, v151, s48, v202
	v_med3_f32 v150, v150, s48, v202
	v_cvt_pk_fp8_f32 v149, v151, v150 op_sel:[0,0,1]
	v_mul_f32_e32 v150, 0x42800000, v32
	v_mul_f32_e32 v151, 0x42800000, v36
	v_med3_f32 v153, v150, s48, v202
	v_med3_f32 v151, v151, s48, v202
	v_mov_b32_e32 v150, v3
	v_cvt_pk_fp8_f32 v150, v153, v151
	v_mul_f32_e32 v152, 0x42800000, v40
	v_mul_f32_e32 v151, 0x42800000, v44
	v_med3_f32 v152, v152, s48, v202
	v_med3_f32 v151, v151, s48, v202
	v_cvt_pk_fp8_f32 v150, v152, v151 op_sel:[0,0,1]
	v_mul_f32_e32 v151, 0x42800000, v48
	v_mul_f32_e32 v152, 0x42800000, v56
	v_med3_f32 v154, v151, s48, v202
	v_med3_f32 v152, v152, s48, v202
	v_mov_b32_e32 v151, v3
	v_cvt_pk_fp8_f32 v151, v154, v152
	v_mul_f32_e32 v153, 0x42800000, v64
	v_mul_f32_e32 v152, 0x42800000, v76
	v_med3_f32 v153, v153, s48, v202
	v_med3_f32 v152, v152, s48, v202
	v_cvt_pk_fp8_f32 v151, v153, v152 op_sel:[0,0,1]
	v_mul_f32_e32 v152, 0x42800000, v105
	v_mul_f32_e32 v153, 0x42800000, v5
	v_med3_f32 v155, v152, s48, v202
	v_med3_f32 v153, v153, s48, v202
	v_mov_b32_e32 v152, v3
	v_cvt_pk_fp8_f32 v152, v155, v153
	v_mul_f32_e32 v154, 0x42800000, v9
	v_mul_f32_e32 v153, 0x42800000, v13
	v_med3_f32 v154, v154, s48, v202
	v_med3_f32 v153, v153, s48, v202
	v_cvt_pk_fp8_f32 v152, v154, v153 op_sel:[0,0,1]
	v_mul_f32_e32 v153, 0x42800000, v17
	v_mul_f32_e32 v154, 0x42800000, v21
	v_med3_f32 v156, v153, s48, v202
	v_med3_f32 v154, v154, s48, v202
	v_mov_b32_e32 v153, v3
	v_cvt_pk_fp8_f32 v153, v156, v154
	v_mul_f32_e32 v155, 0x42800000, v25
	v_mul_f32_e32 v154, 0x42800000, v29
	v_med3_f32 v155, v155, s48, v202
	v_med3_f32 v154, v154, s48, v202
	v_cvt_pk_fp8_f32 v153, v155, v154 op_sel:[0,0,1]
	v_mul_f32_e32 v154, 0x42800000, v33
	v_mul_f32_e32 v155, 0x42800000, v37
	v_med3_f32 v157, v154, s48, v202
	v_med3_f32 v155, v155, s48, v202
	v_mov_b32_e32 v154, v3
	v_cvt_pk_fp8_f32 v154, v157, v155
	v_mul_f32_e32 v156, 0x42800000, v41
	v_mul_f32_e32 v155, 0x42800000, v45
	v_med3_f32 v156, v156, s48, v202
	v_med3_f32 v155, v155, s48, v202
	v_cvt_pk_fp8_f32 v154, v156, v155 op_sel:[0,0,1]
	v_mul_f32_e32 v155, 0x42800000, v49
	v_mul_f32_e32 v156, 0x42800000, v57
	v_med3_f32 v158, v155, s48, v202
	v_med3_f32 v156, v156, s48, v202
	v_mov_b32_e32 v155, v3
	v_cvt_pk_fp8_f32 v155, v158, v156
	v_mul_f32_e32 v157, 0x42800000, v65
	v_mul_f32_e32 v156, 0x42800000, v77
	v_med3_f32 v157, v157, s48, v202
	v_med3_f32 v156, v156, s48, v202
	v_cvt_pk_fp8_f32 v155, v157, v156 op_sel:[0,0,1]
	v_mul_f32_e32 v156, 0x42800000, v106
	v_mul_f32_e32 v157, 0x42800000, v6
	v_med3_f32 v159, v156, s48, v202
	v_med3_f32 v157, v157, s48, v202
	v_mov_b32_e32 v156, v3
	v_cvt_pk_fp8_f32 v156, v159, v157
	v_mul_f32_e32 v158, 0x42800000, v10
	v_mul_f32_e32 v157, 0x42800000, v14
	v_med3_f32 v158, v158, s48, v202
	v_med3_f32 v157, v157, s48, v202
	v_cvt_pk_fp8_f32 v156, v158, v157 op_sel:[0,0,1]
	v_mul_f32_e32 v157, 0x42800000, v18
	v_mul_f32_e32 v158, 0x42800000, v22
	v_med3_f32 v160, v157, s48, v202
	v_med3_f32 v158, v158, s48, v202
	v_mov_b32_e32 v157, v3
	v_cvt_pk_fp8_f32 v157, v160, v158
	v_mul_f32_e32 v159, 0x42800000, v26
	v_mul_f32_e32 v158, 0x42800000, v30
	v_med3_f32 v159, v159, s48, v202
	v_med3_f32 v158, v158, s48, v202
	v_cvt_pk_fp8_f32 v157, v159, v158 op_sel:[0,0,1]
	v_mul_f32_e32 v158, 0x42800000, v34
	v_mul_f32_e32 v159, 0x42800000, v38
	v_med3_f32 v161, v158, s48, v202
	v_med3_f32 v159, v159, s48, v202
	v_mov_b32_e32 v158, v3
	v_cvt_pk_fp8_f32 v158, v161, v159
	v_mul_f32_e32 v160, 0x42800000, v42
	v_mul_f32_e32 v159, 0x42800000, v46
	v_med3_f32 v160, v160, s48, v202
	v_med3_f32 v159, v159, s48, v202
	v_cvt_pk_fp8_f32 v158, v160, v159 op_sel:[0,0,1]
	v_mul_f32_e32 v159, 0x42800000, v50
	v_mul_f32_e32 v160, 0x42800000, v58
	v_med3_f32 v162, v159, s48, v202
	v_med3_f32 v160, v160, s48, v202
	v_mov_b32_e32 v159, v3
	v_cvt_pk_fp8_f32 v159, v162, v160
	v_mul_f32_e32 v161, 0x42800000, v66
	v_mul_f32_e32 v160, 0x42800000, v78
	v_med3_f32 v161, v161, s48, v202
	v_med3_f32 v160, v160, s48, v202
	v_cvt_pk_fp8_f32 v159, v161, v160 op_sel:[0,0,1]
	ds_write_b128 v145, v[148:151]
	ds_write_b128 v145, v[152:155] offset:144
	ds_write_b128 v145, v[156:159] offset:288
	v_mul_f32_e32 v148, 0x42800000, v107
	v_mul_f32_e32 v149, 0x42800000, v7
	v_med3_f32 v151, v148, s48, v202
	v_med3_f32 v149, v149, s48, v202
	v_mov_b32_e32 v148, v3
	v_cvt_pk_fp8_f32 v148, v151, v149
	v_mul_f32_e32 v150, 0x42800000, v11
	v_mul_f32_e32 v149, 0x42800000, v15
	v_med3_f32 v150, v150, s48, v202
	v_med3_f32 v149, v149, s48, v202
	v_cvt_pk_fp8_f32 v148, v150, v149 op_sel:[0,0,1]
	v_mul_f32_e32 v149, 0x42800000, v19
	v_mul_f32_e32 v150, 0x42800000, v23
	v_med3_f32 v152, v149, s48, v202
	v_med3_f32 v150, v150, s48, v202
	v_mov_b32_e32 v149, v3
	v_cvt_pk_fp8_f32 v149, v152, v150
	v_mul_f32_e32 v151, 0x42800000, v27
	v_mul_f32_e32 v150, 0x42800000, v31
	v_med3_f32 v151, v151, s48, v202
	v_med3_f32 v150, v150, s48, v202
	v_cvt_pk_fp8_f32 v149, v151, v150 op_sel:[0,0,1]
	v_mul_f32_e32 v150, 0x42800000, v35
	v_mul_f32_e32 v151, 0x42800000, v39
	v_med3_f32 v153, v150, s48, v202
	v_med3_f32 v151, v151, s48, v202
	v_mov_b32_e32 v150, v3
	v_cvt_pk_fp8_f32 v150, v153, v151
	v_mul_f32_e32 v152, 0x42800000, v43
	v_mul_f32_e32 v151, 0x42800000, v47
	v_med3_f32 v152, v152, s48, v202
	v_med3_f32 v151, v151, s48, v202
	v_cvt_pk_fp8_f32 v150, v152, v151 op_sel:[0,0,1]
	v_mul_f32_e32 v151, 0x42800000, v51
	v_mul_f32_e32 v152, 0x42800000, v59
	v_med3_f32 v154, v151, s48, v202
	v_med3_f32 v152, v152, s48, v202
	v_mov_b32_e32 v151, v3
	v_cvt_pk_fp8_f32 v151, v154, v152
	v_mul_f32_e32 v153, 0x42800000, v67
	v_mul_f32_e32 v152, 0x42800000, v79
	v_med3_f32 v153, v153, s48, v202
	v_med3_f32 v152, v152, s48, v202
	v_cvt_pk_fp8_f32 v151, v153, v152 op_sel:[0,0,1]
	v_cndmask_b32_e64 v152, 0, 1, s[84:85]
	v_cmp_ne_u32_e64 s[24:25], 1, v152
	s_andn2_b64 vcc, exec, s[84:85]
	ds_write_b128 v145, v[148:151] offset:432
	s_cbranch_vccnz .Lcv3_nomore
	s_lshl_b64 s[68:69], s[44:45], 2
	v_lshl_add_u64 v[4:5], v[132:133], 0, s[68:69]
	v_lshl_add_u64 v[12:13], v[4:5], 0, s[68:69]
	global_load_dwordx4 v[104:107], v[132:133], off
	s_nop 0
	global_load_dwordx4 v[4:7], v[4:5], off
	s_nop 0
	global_load_dwordx4 v[8:11], v[12:13], off
	v_lshl_add_u64 v[12:13], v[12:13], 0, s[68:69]
	v_lshl_add_u64 v[20:21], v[12:13], 0, s[68:69]
	global_load_dwordx4 v[12:15], v[12:13], off
	s_nop 0
	global_load_dwordx4 v[16:19], v[20:21], off
	v_lshl_add_u64 v[20:21], v[20:21], 0, s[68:69]
	v_lshl_add_u64 v[28:29], v[20:21], 0, s[68:69]
	global_load_dwordx4 v[20:23], v[20:21], off
	s_nop 0
	global_load_dwordx4 v[24:27], v[28:29], off
	v_lshl_add_u64 v[28:29], v[28:29], 0, s[68:69]
	v_lshl_add_u64 v[36:37], v[28:29], 0, s[68:69]
	global_load_dwordx4 v[28:31], v[28:29], off
	s_nop 0
	global_load_dwordx4 v[32:35], v[36:37], off
	v_lshl_add_u64 v[36:37], v[36:37], 0, s[68:69]
	v_lshl_add_u64 v[44:45], v[36:37], 0, s[68:69]
	v_lshl_add_u64 v[48:49], v[44:45], 0, s[68:69]
	v_lshl_add_u64 v[56:57], v[48:49], 0, s[68:69]
	v_lshl_add_u64 v[64:65], v[56:57], 0, s[68:69]
	v_lshl_add_u64 v[76:77], v[64:65], 0, s[68:69]
	global_load_dwordx4 v[36:39], v[36:37], off
	s_nop 0
	global_load_dwordx4 v[40:43], v[44:45], off
	s_nop 0
	global_load_dwordx4 v[44:47], v[48:49], off
	s_nop 0
	global_load_dwordx4 v[48:51], v[56:57], off
	s_nop 0
	global_load_dwordx4 v[56:59], v[64:65], off
	s_nop 0
	global_load_dwordx4 v[64:67], v[76:77], off
	v_lshl_add_u64 v[76:77], v[76:77], 0, s[68:69]
	global_load_dwordx4 v[76:79], v[76:77], off
	s_waitcnt vmcnt(16)
	s_branch .LBB0_343

.LBB0_343:
	v_mul_f32_e32 v148, 0x42800000, v52
	v_mul_f32_e32 v149, 0x42800000, v60
	v_med3_f32 v151, v148, s48, v202
	v_med3_f32 v149, v149, s48, v202
	v_mov_b32_e32 v148, 0
	v_cvt_pk_fp8_f32 v148, v151, v149
	v_mul_f32_e32 v150, 0x42800000, v68
	v_mul_f32_e32 v149, 0x42800000, v72
	v_med3_f32 v150, v150, s48, v202
	v_med3_f32 v149, v149, s48, v202
	v_cvt_pk_fp8_f32 v148, v150, v149 op_sel:[0,0,1]
	v_mul_f32_e32 v149, 0x42800000, v80
	v_mul_f32_e32 v150, 0x42800000, v84
	v_med3_f32 v152, v149, s48, v202
	v_med3_f32 v150, v150, s48, v202
	v_mov_b32_e32 v149, 0
	v_cvt_pk_fp8_f32 v149, v152, v150
	v_mul_f32_e32 v151, 0x42800000, v88
	v_mul_f32_e32 v150, 0x42800000, v92
	v_med3_f32 v151, v151, s48, v202
	v_med3_f32 v150, v150, s48, v202
	v_cvt_pk_fp8_f32 v149, v151, v150 op_sel:[0,0,1]
	v_mul_f32_e32 v150, 0x42800000, v96
	v_mul_f32_e32 v151, 0x42800000, v100
	v_med3_f32 v153, v150, s48, v202
	v_med3_f32 v151, v151, s48, v202
	v_mov_b32_e32 v150, 0
	v_cvt_pk_fp8_f32 v150, v153, v151
	v_mul_f32_e32 v152, 0x42800000, v108
	v_mul_f32_e32 v151, 0x42800000, v112
	v_med3_f32 v152, v152, s48, v202
	v_med3_f32 v151, v151, s48, v202
	v_cvt_pk_fp8_f32 v150, v152, v151 op_sel:[0,0,1]
	v_mul_f32_e32 v151, 0x42800000, v116
	v_mul_f32_e32 v152, 0x42800000, v120
	v_med3_f32 v154, v151, s48, v202
	v_med3_f32 v152, v152, s48, v202
	v_mov_b32_e32 v151, 0
	v_cvt_pk_fp8_f32 v151, v154, v152
	v_mul_f32_e32 v153, 0x42800000, v124
	s_nop 0
	v_mul_f32_e32 v152, 0x42800000, v128
	v_med3_f32 v153, v153, s48, v202
	v_med3_f32 v152, v152, s48, v202
	v_cvt_pk_fp8_f32 v151, v153, v152 op_sel:[0,0,1]
	s_and_b64 vcc, exec, s[24:25]
	ds_write_b128 v146, v[148:151] offset:64
	v_mul_f32_e32 v148, 0x42800000, v53
	v_mul_f32_e32 v149, 0x42800000, v61
	v_med3_f32 v151, v148, s48, v202
	v_med3_f32 v149, v149, s48, v202
	v_mov_b32_e32 v148, 0
	v_cvt_pk_fp8_f32 v148, v151, v149
	v_mul_f32_e32 v150, 0x42800000, v69
	v_mul_f32_e32 v149, 0x42800000, v73
	v_med3_f32 v150, v150, s48, v202
	v_med3_f32 v149, v149, s48, v202
	v_cvt_pk_fp8_f32 v148, v150, v149 op_sel:[0,0,1]
	v_mul_f32_e32 v149, 0x42800000, v81
	v_mul_f32_e32 v150, 0x42800000, v85
	v_med3_f32 v152, v149, s48, v202
	v_med3_f32 v150, v150, s48, v202
	v_mov_b32_e32 v149, 0
	v_cvt_pk_fp8_f32 v149, v152, v150
	v_mul_f32_e32 v151, 0x42800000, v89
	v_mul_f32_e32 v150, 0x42800000, v93
	v_med3_f32 v151, v151, s48, v202
	v_med3_f32 v150, v150, s48, v202
	v_cvt_pk_fp8_f32 v149, v151, v150 op_sel:[0,0,1]
	v_mul_f32_e32 v150, 0x42800000, v97
	v_mul_f32_e32 v151, 0x42800000, v101
	v_med3_f32 v153, v150, s48, v202
	v_med3_f32 v151, v151, s48, v202
	v_mov_b32_e32 v150, 0
	v_cvt_pk_fp8_f32 v150, v153, v151
	v_mul_f32_e32 v152, 0x42800000, v109
	v_mul_f32_e32 v151, 0x42800000, v113
	v_med3_f32 v152, v152, s48, v202
	v_med3_f32 v151, v151, s48, v202
	v_cvt_pk_fp8_f32 v150, v152, v151 op_sel:[0,0,1]
	v_mul_f32_e32 v151, 0x42800000, v117
	v_mul_f32_e32 v152, 0x42800000, v121
	v_med3_f32 v154, v151, s48, v202
	v_med3_f32 v152, v152, s48, v202
	v_mov_b32_e32 v151, 0
	v_cvt_pk_fp8_f32 v151, v154, v152
	v_mul_f32_e32 v153, 0x42800000, v125
	v_mul_f32_e32 v152, 0x42800000, v129
	v_med3_f32 v153, v153, s48, v202
	v_med3_f32 v152, v152, s48, v202
	v_cvt_pk_fp8_f32 v151, v153, v152 op_sel:[0,0,1]
	v_mul_f32_e32 v152, 0x42800000, v54
	v_mul_f32_e32 v153, 0x42800000, v62
	v_med3_f32 v155, v152, s48, v202
	v_med3_f32 v153, v153, s48, v202
	v_mov_b32_e32 v152, 0
	v_cvt_pk_fp8_f32 v152, v155, v153
	v_mul_f32_e32 v154, 0x42800000, v70
	v_mul_f32_e32 v153, 0x42800000, v74
	v_med3_f32 v154, v154, s48, v202
	v_med3_f32 v153, v153, s48, v202
	v_cvt_pk_fp8_f32 v152, v154, v153 op_sel:[0,0,1]
	v_mul_f32_e32 v153, 0x42800000, v82
	v_mul_f32_e32 v154, 0x42800000, v86
	v_med3_f32 v156, v153, s48, v202
	v_med3_f32 v154, v154, s48, v202
	v_mov_b32_e32 v153, 0
	v_cvt_pk_fp8_f32 v153, v156, v154
	v_mul_f32_e32 v155, 0x42800000, v90
	v_mul_f32_e32 v154, 0x42800000, v94
	v_med3_f32 v155, v155, s48, v202
	v_med3_f32 v154, v154, s48, v202
	v_cvt_pk_fp8_f32 v153, v155, v154 op_sel:[0,0,1]
	v_mul_f32_e32 v154, 0x42800000, v98
	v_mul_f32_e32 v155, 0x42800000, v102
	v_med3_f32 v157, v154, s48, v202
	v_med3_f32 v155, v155, s48, v202
	v_mov_b32_e32 v154, 0
	v_cvt_pk_fp8_f32 v154, v157, v155
	v_mul_f32_e32 v156, 0x42800000, v110
	v_mul_f32_e32 v155, 0x42800000, v114
	v_med3_f32 v156, v156, s48, v202
	v_med3_f32 v155, v155, s48, v202
	v_cvt_pk_fp8_f32 v154, v156, v155 op_sel:[0,0,1]
	v_mul_f32_e32 v155, 0x42800000, v118
	v_mul_f32_e32 v156, 0x42800000, v122
	v_med3_f32 v158, v155, s48, v202
	v_med3_f32 v156, v156, s48, v202
	v_mov_b32_e32 v155, 0
	v_cvt_pk_fp8_f32 v155, v158, v156
	v_mul_f32_e32 v157, 0x42800000, v126
	v_mul_f32_e32 v156, 0x42800000, v130
	v_med3_f32 v157, v157, s48, v202
	v_med3_f32 v156, v156, s48, v202
	v_cvt_pk_fp8_f32 v155, v157, v156 op_sel:[0,0,1]
	v_mul_f32_e32 v156, 0x42800000, v55
	v_mul_f32_e32 v157, 0x42800000, v63
	v_med3_f32 v159, v156, s48, v202
	v_med3_f32 v157, v157, s48, v202
	v_mov_b32_e32 v156, 0
	v_cvt_pk_fp8_f32 v156, v159, v157
	v_mul_f32_e32 v158, 0x42800000, v71
	v_mul_f32_e32 v157, 0x42800000, v75
	v_med3_f32 v158, v158, s48, v202
	v_med3_f32 v157, v157, s48, v202
	v_cvt_pk_fp8_f32 v156, v158, v157 op_sel:[0,0,1]
	v_mul_f32_e32 v157, 0x42800000, v83
	v_mul_f32_e32 v158, 0x42800000, v87
	v_med3_f32 v160, v157, s48, v202
	v_med3_f32 v158, v158, s48, v202
	v_mov_b32_e32 v157, 0
	v_cvt_pk_fp8_f32 v157, v160, v158
	v_mul_f32_e32 v159, 0x42800000, v91
	v_mul_f32_e32 v158, 0x42800000, v95
	v_med3_f32 v159, v159, s48, v202
	v_med3_f32 v158, v158, s48, v202
	v_cvt_pk_fp8_f32 v157, v159, v158 op_sel:[0,0,1]
	v_mul_f32_e32 v158, 0x42800000, v99
	v_mul_f32_e32 v159, 0x42800000, v103
	v_med3_f32 v161, v158, s48, v202
	v_med3_f32 v159, v159, s48, v202
	v_mov_b32_e32 v158, 0
	v_cvt_pk_fp8_f32 v158, v161, v159
	v_mul_f32_e32 v160, 0x42800000, v111
	v_mul_f32_e32 v159, 0x42800000, v115
	v_med3_f32 v160, v160, s48, v202
	v_med3_f32 v159, v159, s48, v202
	v_cvt_pk_fp8_f32 v158, v160, v159 op_sel:[0,0,1]
	v_mul_f32_e32 v159, 0x42800000, v119
	v_mul_f32_e32 v160, 0x42800000, v123
	v_med3_f32 v162, v159, s48, v202
	v_med3_f32 v160, v160, s48, v202
	v_mov_b32_e32 v159, 0
	v_cvt_pk_fp8_f32 v159, v162, v160
	v_mul_f32_e32 v161, 0x42800000, v127
	v_mul_f32_e32 v160, 0x42800000, v131
	v_med3_f32 v161, v161, s48, v202
	v_med3_f32 v160, v160, s48, v202
	v_cvt_pk_fp8_f32 v159, v161, v160 op_sel:[0,0,1]
	ds_write_b128 v146, v[148:151] offset:208
	ds_write_b128 v146, v[152:155] offset:352
	ds_write_b128 v146, v[156:159] offset:496
	s_cbranch_vccnz .LBB0_333
	s_lshl_b64 s[24:25], s[44:45], 8
	v_lshl_add_u64 v[52:53], v[132:133], 0, s[24:25]
	s_lshl_b64 s[24:25], s[44:45], 2
	v_lshl_add_u64 v[68:69], v[52:53], 0, s[24:25]
	global_load_dwordx4 v[52:55], v[52:53], off
	s_nop 0
	global_load_dwordx4 v[60:63], v[68:69], off
	v_lshl_add_u64 v[68:69], v[68:69], 0, s[24:25]
	v_lshl_add_u64 v[80:81], v[68:69], 0, s[24:25]
	global_load_dwordx4 v[68:71], v[68:69], off
	s_nop 0
	global_load_dwordx4 v[72:75], v[80:81], off
	v_lshl_add_u64 v[80:81], v[80:81], 0, s[24:25]
	v_lshl_add_u64 v[88:89], v[80:81], 0, s[24:25]
	global_load_dwordx4 v[80:83], v[80:81], off
	s_nop 0
	global_load_dwordx4 v[84:87], v[88:89], off
	v_lshl_add_u64 v[88:89], v[88:89], 0, s[24:25]
	v_lshl_add_u64 v[96:97], v[88:89], 0, s[24:25]
	global_load_dwordx4 v[88:91], v[88:89], off
	s_nop 0
	global_load_dwordx4 v[92:95], v[96:97], off
	v_lshl_add_u64 v[96:97], v[96:97], 0, s[24:25]
	v_lshl_add_u64 v[108:109], v[96:97], 0, s[24:25]
	v_lshl_add_u64 v[112:113], v[108:109], 0, s[24:25]
	v_lshl_add_u64 v[116:117], v[112:113], 0, s[24:25]
	v_lshl_add_u64 v[120:121], v[116:117], 0, s[24:25]
	v_lshl_add_u64 v[124:125], v[120:121], 0, s[24:25]
	v_lshl_add_u64 v[128:129], v[124:125], 0, s[24:25]
	global_load_dwordx4 v[96:99], v[96:97], off
	s_nop 0
	global_load_dwordx4 v[100:103], v[108:109], off
	s_nop 0
	global_load_dwordx4 v[108:111], v[112:113], off
	s_nop 0
	global_load_dwordx4 v[112:115], v[116:117], off
	s_nop 0
	global_load_dwordx4 v[116:119], v[120:121], off
	s_nop 0
	global_load_dwordx4 v[120:123], v[124:125], off
	s_nop 0
	global_load_dwordx4 v[124:127], v[128:129], off
	v_lshl_add_u64 v[128:129], v[128:129], 0, s[24:25]
	global_load_dwordx4 v[128:131], v[128:129], off
	s_branch .LBB0_333
